# attention<0>: one static priority raise (s_setprio 1) for waves 4-7 for the duration of each tile loop
# baseline (speedup 1.0000x reference)
.LBB0_1252:
	s_and_b64 s[18:19], s[16:17], exec
	s_cselect_b32 s29, s26, s27
	s_lshl_b32 s18, s29, 6
	s_add_i32 s18, s18, s28
	v_or_b32_e32 v214, s18, v245
	v_mov_b64_e32 v[0:1], s[2:3]
	v_mad_i64_i32 v[2:3], s[30:31], v214, s96, v[0:1]
	v_lshl_add_u64 v[2:3], v[2:3], 0, s[14:15]
	v_mov_b32_e32 v191, v33
	v_or_b32_e32 v212, 16, v214
	v_lshl_add_u64 v[2:3], v[2:3], 0, v[190:191]
	s_mov_b64 s[34:35], 0x5000
	v_mad_i64_i32 v[0:1], s[30:31], v212, s96, v[0:1]
	v_lshl_add_u64 v[4:5], v[2:3], 0, s[34:35]
	v_add_co_u32_e32 v2, vcc, 0x5000, v2
	v_lshl_add_u64 v[0:1], v[0:1], 0, s[14:15]
	s_nop 0
	v_addc_co_u32_e32 v3, vcc, 0, v3, vcc
	v_lshl_add_u64 v[0:1], v[0:1], 0, v[190:191]
	s_mov_b32 m0, s21
	global_load_dwordx4 v[70:73], v[4:5], off offset:64
	global_load_dwordx4 v[74:77], v[4:5], off offset:128
	global_load_dwordx4 v[78:81], v[2:3], off
	global_load_dwordx4 v[82:85], v[4:5], off offset:192
	v_lshl_add_u64 v[2:3], v[0:1], 0, s[34:35]
	v_add_co_u32_e32 v0, vcc, 0x5000, v0
	s_ashr_i32 s19, s18, 31
	s_nop 0
	v_addc_co_u32_e32 v1, vcc, 0, v1, vcc
	global_load_dwordx4 v[86:89], v[2:3], off offset:64
	global_load_dwordx4 v[90:93], v[2:3], off offset:128
	global_load_dwordx4 v[94:97], v[0:1], off
	global_load_dwordx4 v[98:101], v[2:3], off offset:192
	s_barrier
	global_load_lds_dwordx4 v32, s[0:1]
	s_add_i32 m0, s21, 0x8000
	s_lshl_b64 s[18:19], s[18:19], 9
	global_load_lds_dwordx4 v184, s[0:1]
	s_add_i32 m0, s21, 0x400
	s_nop 0
	global_load_lds_dwordx4 v186, s[0:1]
	s_mov_b32 m0, s22
	s_nop 0
	global_load_lds_dwordx4 v188, s[0:1]
	s_add_u32 s18, s24, s18
	s_addc_u32 s19, s25, s19
	v_lshl_add_u64 v[0:1], s[18:19], 0, v[168:169]
	v_lshl_add_u64 v[2:3], s[18:19], 0, v[174:175]
	global_load_dwordx4 v[24:27], v[0:1], off
	global_load_dwordx4 v[28:31], v[2:3], off
	v_lshl_add_u64 v[0:1], s[18:19], 0, v[176:177]
	v_lshl_add_u64 v[2:3], s[18:19], 0, v[178:179]
	global_load_dwordx4 v[38:41], v[0:1], off
	global_load_dwordx4 v[42:45], v[2:3], off
	s_waitcnt vmcnt(0)
	v_add_u32_e32 v46, 0, v168
	v_add_u32_e32 v46, 0x10000, v46
	s_add_u32 s100, s0, 0x240000
	s_addc_u32 s101, s1, 0
	v_mov_b32_e32 v3, 0
	v_mov_b32_e32 v2, 0
	v_mov_b32_e32 v1, 0
	v_mov_b32_e32 v0, 0
	v_mov_b32_e32 v7, 0
	v_mov_b32_e32 v6, 0
	v_mov_b32_e32 v5, 0
	v_mov_b32_e32 v4, 0
	v_mov_b32_e32 v11, 0
	v_mov_b32_e32 v10, 0
	v_mov_b32_e32 v9, 0
	v_mov_b32_e32 v8, 0
	v_mov_b32_e32 v15, 0
	v_mov_b32_e32 v14, 0
	v_mov_b32_e32 v13, 0
	v_mov_b32_e32 v12, 0
	v_mov_b32_e32 v19, 0
	v_mov_b32_e32 v18, 0
	v_mov_b32_e32 v17, 0
	v_mov_b32_e32 v16, 0
	v_mov_b32_e32 v23, 0
	v_mov_b32_e32 v22, 0
	v_mov_b32_e32 v21, 0
	v_mov_b32_e32 v20, 0
	s_cmp_lt_i32 s29, 0
	v_mov_b32_e32 v49, 0
	v_mov_b32_e32 v48, 0
	v_mov_b32_e32 v47, 0
	v_mov_b32_e32 v53, 0
	v_mov_b32_e32 v52, 0
	v_mov_b32_e32 v51, 0
	v_mov_b32_e32 v50, 0
	v_mov_b32_e32 v57, 0
	v_mov_b32_e32 v56, 0
	v_mov_b32_e32 v55, 0
	v_mov_b32_e32 v54, 0
	v_mov_b32_e32 v61, 0
	v_mov_b32_e32 v60, 0
	v_mov_b32_e32 v59, 0
	v_mov_b32_e32 v58, 0
	v_mov_b32_e32 v65, 0
	ds_write_b128 v46, v[24:27]
	ds_write_b128 v46, v[28:31] offset:8192
	ds_write_b128 v46, v[38:41] offset:16384
	ds_write_b128 v46, v[42:45] offset:24576
	s_waitcnt vmcnt(0)
	v_mov_b32_e32 v27, 0
	v_mov_b32_e32 v26, 0
	v_mov_b32_e32 v25, 0
	v_mov_b32_e32 v24, 0
	v_mov_b32_e32 v31, 0
	v_mov_b32_e32 v30, 0
	v_mov_b32_e32 v29, 0
	v_mov_b32_e32 v28, 0
	v_mov_b32_e32 v41, 0
	v_mov_b32_e32 v40, 0
	v_mov_b32_e32 v39, 0
	v_mov_b32_e32 v38, 0
	v_mov_b32_e32 v45, 0
	v_mov_b32_e32 v44, 0
	v_mov_b32_e32 v43, 0
	v_mov_b32_e32 v42, 0
	v_mov_b32_e32 v46, 0
	v_mov_b32_e32 v64, 0
	v_mov_b32_e32 v63, 0
	v_mov_b32_e32 v62, 0
	v_mov_b32_e32 v69, 0
	v_mov_b32_e32 v68, 0
	v_mov_b32_e32 v67, 0
	v_mov_b32_e32 v66, 0
	v_mov_b32_e32 v102, 0
	v_mov_b32_e32 v103, 0
	s_waitcnt vmcnt(0) lgkmcnt(0)
	s_barrier
	s_cbranch_scc1 .LBB0_1251
	v_readfirstlane_b32 s18, v219
	s_bitcmp1_b32 s18, 8
	s_cbranch_scc0 .Lat0_np
	s_setprio 1
.Lat0_np:
	v_mov_b32_e32 v66, v33
	v_mov_b32_e32 v67, v33
	v_mov_b32_e32 v68, v33
	v_mov_b32_e32 v69, v33
	v_mov_b64_e32 v[62:63], v[66:67]
	v_mov_b64_e32 v[58:59], v[66:67]
	v_mov_b64_e32 v[54:55], v[66:67]
	v_mov_b64_e32 v[50:51], v[66:67]
	v_mov_b64_e32 v[46:47], v[66:67]
	v_mov_b64_e32 v[42:43], v[66:67]
	v_mov_b64_e32 v[38:39], v[66:67]
	v_mov_b64_e32 v[28:29], v[66:67]
	v_mov_b64_e32 v[24:25], v[66:67]
	v_mov_b64_e32 v[20:21], v[66:67]
	v_mov_b64_e32 v[16:17], v[66:67]
	v_mov_b64_e32 v[12:13], v[66:67]
	v_mov_b64_e32 v[8:9], v[66:67]
	v_mov_b64_e32 v[4:5], v[66:67]
	v_mov_b64_e32 v[0:1], v[66:67]
	s_add_i32 s30, s29, 1
	s_mov_b32 s31, 0
	v_mov_b32_e32 v218, 0xf149f2ca
	v_mov_b32_e32 v215, 0
	v_mov_b32_e32 v213, v246
	v_mov_b32_e32 v248, 0
	v_mov_b32_e32 v167, 0xf149f2ca
	v_mov_b64_e32 v[64:65], v[68:69]
	v_mov_b64_e32 v[60:61], v[68:69]
	v_mov_b64_e32 v[56:57], v[68:69]
	v_mov_b64_e32 v[52:53], v[68:69]
	v_mov_b64_e32 v[48:49], v[68:69]
	v_mov_b64_e32 v[44:45], v[68:69]
	v_mov_b64_e32 v[40:41], v[68:69]
	v_mov_b64_e32 v[30:31], v[68:69]
	v_mov_b64_e32 v[26:27], v[68:69]
	v_mov_b64_e32 v[22:23], v[68:69]
	v_mov_b64_e32 v[18:19], v[68:69]
	v_mov_b64_e32 v[14:15], v[68:69]
	v_mov_b64_e32 v[10:11], v[68:69]
	v_mov_b64_e32 v[6:7], v[68:69]
	v_mov_b64_e32 v[2:3], v[68:69]
	s_and_b32 s34, s31, 1
	s_cmp_lt_i32 s31, s29
	s_mov_b64 s[18:19], -1
	s_cbranch_scc1 .LBB0_1256
	s_branch .LBB0_1255

.LBB0_1262:
	v_cvt_pk_bf16_f32 v162, v162, v163
	v_cvt_pk_bf16_f32 v163, v164, v165
	v_cvt_pk_bf16_f32 v164, v158, v159
	v_cvt_pk_bf16_f32 v165, v160, v161
	v_cvt_pk_bf16_f32 v158, v218, v167
	v_cvt_pk_bf16_f32 v159, v136, v135
	v_cvt_pk_bf16_f32 v160, v138, v137
	v_cvt_pk_bf16_f32 v161, v140, v139
	v_mfma_f32_16x16x32_bf16 v[54:57], v[106:109], v[162:165], v[54:57]
	v_cvt_pk_bf16_f32 v154, v154, v155
	v_cvt_pk_bf16_f32 v155, v216, v157
	v_cvt_pk_bf16_f32 v156, v156, v151
	v_mfma_f32_16x16x32_bf16 v[16:19], v[106:109], v[158:161], v[16:19]
	v_cvt_pk_bf16_f32 v157, v152, v153
	s_add_i32 s31, s31, 1
	v_mfma_f32_16x16x32_bf16 v[66:69], v[130:133], v[162:165], v[66:69]
	v_add_u32_e32 v213, 8, v213
	s_cmp_eq_u32 s30, s31
	v_mfma_f32_16x16x32_bf16 v[28:31], v[130:133], v[158:161], v[28:31]
	v_cvt_pk_bf16_f32 v130, v146, v141
	v_cvt_pk_bf16_f32 v131, v148, v147
	v_cvt_pk_bf16_f32 v132, v142, v143
	v_cvt_pk_bf16_f32 v133, v144, v145
	v_mfma_f32_16x16x32_bf16 v[54:57], v[102:105], v[154:157], v[54:57]
	s_nop 0
	v_mfma_f32_16x16x32_bf16 v[16:19], v[102:105], v[130:133], v[16:19]
	ds_read_b64_tr_b16 v[102:103], v241 offset:32768
	ds_read_b64_tr_b16 v[104:105], v241 offset:36864
	ds_read_b64_tr_b16 v[106:107], v241 offset:40960
	ds_read_b64_tr_b16 v[108:109], v241 offset:45056
	v_mfma_f32_16x16x32_bf16 v[58:61], v[118:121], v[162:165], v[58:61]
	v_mfma_f32_16x16x32_bf16 v[20:23], v[118:121], v[158:161], v[20:23]
	s_waitcnt lgkmcnt(2)
	v_mfma_f32_16x16x32_bf16 v[50:53], v[102:105], v[162:165], v[50:53]
	v_mfma_f32_16x16x32_bf16 v[12:15], v[102:105], v[158:161], v[12:15]
	v_mfma_f32_16x16x32_bf16 v[58:61], v[110:113], v[154:157], v[58:61]
	v_mfma_f32_16x16x32_bf16 v[20:23], v[110:113], v[130:133], v[20:23]
	s_waitcnt lgkmcnt(0)
	v_mfma_f32_16x16x32_bf16 v[50:53], v[106:109], v[154:157], v[50:53]
	v_mfma_f32_16x16x32_bf16 v[12:15], v[106:109], v[130:133], v[12:15]
	ds_read_b64_tr_b16 v[102:103], v242 offset:32768
	ds_read_b64_tr_b16 v[104:105], v242 offset:36864
	ds_read_b64_tr_b16 v[106:107], v242 offset:40960
	ds_read_b64_tr_b16 v[108:109], v242 offset:45056
	s_waitcnt lgkmcnt(2)
	v_mfma_f32_16x16x32_bf16 v[46:49], v[102:105], v[162:165], v[46:49]
	v_mfma_f32_16x16x32_bf16 v[8:11], v[102:105], v[158:161], v[8:11]
	s_waitcnt lgkmcnt(0)
	v_mfma_f32_16x16x32_bf16 v[46:49], v[106:109], v[154:157], v[46:49]
	v_mfma_f32_16x16x32_bf16 v[8:11], v[106:109], v[130:133], v[8:11]
	ds_read_b64_tr_b16 v[102:103], v243 offset:32768
	ds_read_b64_tr_b16 v[104:105], v243 offset:36864
	ds_read_b64_tr_b16 v[106:107], v243 offset:40960
	ds_read_b64_tr_b16 v[108:109], v243 offset:45056
	s_waitcnt lgkmcnt(2)
	v_mfma_f32_16x16x32_bf16 v[42:45], v[102:105], v[162:165], v[42:45]
	v_mfma_f32_16x16x32_bf16 v[4:7], v[102:105], v[158:161], v[4:7]
	ds_read_b64_tr_b16 v[110:111], v244 offset:32768
	ds_read_b64_tr_b16 v[112:113], v244 offset:36864
	s_waitcnt lgkmcnt(2)
	v_mfma_f32_16x16x32_bf16 v[42:45], v[106:109], v[154:157], v[42:45]
	v_mfma_f32_16x16x32_bf16 v[4:7], v[106:109], v[130:133], v[4:7]
	ds_read_b64_tr_b16 v[104:105], v244 offset:40960
	ds_read_b64_tr_b16 v[106:107], v244 offset:45056
	s_waitcnt vmcnt(0)
	v_mfma_f32_16x16x32_bf16 v[62:65], v[126:129], v[162:165], v[62:65]
	s_waitcnt lgkmcnt(0)
	s_barrier
	v_mfma_f32_16x16x32_bf16 v[24:27], v[126:129], v[158:161], v[24:27]
	v_mfma_f32_16x16x32_bf16 v[38:41], v[110:113], v[162:165], v[38:41]
	v_mfma_f32_16x16x32_bf16 v[0:3], v[110:113], v[158:161], v[0:3]
	v_mfma_f32_16x16x32_bf16 v[66:69], v[122:125], v[154:157], v[66:69]
	v_mfma_f32_16x16x32_bf16 v[28:31], v[122:125], v[130:133], v[28:31]
	v_mfma_f32_16x16x32_bf16 v[62:65], v[114:117], v[154:157], v[62:65]
	v_mfma_f32_16x16x32_bf16 v[24:27], v[114:117], v[130:133], v[24:27]
	v_mfma_f32_16x16x32_bf16 v[38:41], v[104:107], v[154:157], v[38:41]
	v_mfma_f32_16x16x32_bf16 v[0:3], v[104:107], v[130:133], v[0:3]
	s_cbranch_scc0 .Lat0_O_1254
	v_mov_b32_e32 v189, v215
	v_mov_b32_e32 v198, v248
	s_nop 1
	v_permlane16_swap_b32_e32 v215, v189
	v_permlane16_swap_b32_e32 v248, v198
	v_add_f32_e32 v189, v215, v189
	v_add_f32_e32 v198, v248, v198
	v_mov_b32_e32 v217, v189
	v_mov_b32_e32 v250, v198
	s_nop 1
	v_permlane32_swap_b32_e32 v189, v217
	v_permlane32_swap_b32_e32 v198, v250
	v_add_f32_e32 v103, v189, v217
	v_add_f32_e32 v102, v198, v250
	s_setprio 0
	s_branch .LBB0_1251

.Lat0_O_1262:
	v_cvt_pk_bf16_f32 v162, v162, v163
	v_cvt_pk_bf16_f32 v163, v164, v165
	v_cvt_pk_bf16_f32 v164, v158, v159
	v_cvt_pk_bf16_f32 v165, v160, v161
	v_cvt_pk_bf16_f32 v158, v218, v167
	v_cvt_pk_bf16_f32 v159, v136, v135
	v_cvt_pk_bf16_f32 v160, v138, v137
	v_cvt_pk_bf16_f32 v161, v140, v139
	v_mfma_f32_16x16x32_bf16 v[54:57], v[106:109], v[162:165], v[54:57]
	v_cvt_pk_bf16_f32 v154, v154, v155
	v_cvt_pk_bf16_f32 v155, v216, v157
	v_cvt_pk_bf16_f32 v156, v156, v151
	v_mfma_f32_16x16x32_bf16 v[16:19], v[106:109], v[158:161], v[16:19]
	v_cvt_pk_bf16_f32 v157, v152, v153
	s_add_i32 s31, s31, 1
	v_mfma_f32_16x16x32_bf16 v[66:69], v[130:133], v[162:165], v[66:69]
	v_add_u32_e32 v213, 8, v213
	s_cmp_eq_u32 s30, s31
	v_mfma_f32_16x16x32_bf16 v[28:31], v[130:133], v[158:161], v[28:31]
	v_cvt_pk_bf16_f32 v130, v146, v141
	v_cvt_pk_bf16_f32 v131, v148, v147
	v_cvt_pk_bf16_f32 v132, v142, v143
	v_cvt_pk_bf16_f32 v133, v144, v145
	v_mfma_f32_16x16x32_bf16 v[54:57], v[102:105], v[154:157], v[54:57]
	s_nop 0
	v_mfma_f32_16x16x32_bf16 v[16:19], v[102:105], v[130:133], v[16:19]
	ds_read_b64_tr_b16 v[102:103], v241 offset:49152
	ds_read_b64_tr_b16 v[104:105], v241 offset:53248
	ds_read_b64_tr_b16 v[106:107], v241 offset:57344
	ds_read_b64_tr_b16 v[108:109], v241 offset:61440
	v_mfma_f32_16x16x32_bf16 v[58:61], v[118:121], v[162:165], v[58:61]
	v_mfma_f32_16x16x32_bf16 v[20:23], v[118:121], v[158:161], v[20:23]
	s_waitcnt lgkmcnt(2)
	v_mfma_f32_16x16x32_bf16 v[50:53], v[102:105], v[162:165], v[50:53]
	v_mfma_f32_16x16x32_bf16 v[12:15], v[102:105], v[158:161], v[12:15]
	v_mfma_f32_16x16x32_bf16 v[58:61], v[110:113], v[154:157], v[58:61]
	v_mfma_f32_16x16x32_bf16 v[20:23], v[110:113], v[130:133], v[20:23]
	s_waitcnt lgkmcnt(0)
	v_mfma_f32_16x16x32_bf16 v[50:53], v[106:109], v[154:157], v[50:53]
	v_mfma_f32_16x16x32_bf16 v[12:15], v[106:109], v[130:133], v[12:15]
	ds_read_b64_tr_b16 v[102:103], v242 offset:49152
	ds_read_b64_tr_b16 v[104:105], v242 offset:53248
	ds_read_b64_tr_b16 v[106:107], v242 offset:57344
	ds_read_b64_tr_b16 v[108:109], v242 offset:61440
	s_waitcnt lgkmcnt(2)
	v_mfma_f32_16x16x32_bf16 v[46:49], v[102:105], v[162:165], v[46:49]
	v_mfma_f32_16x16x32_bf16 v[8:11], v[102:105], v[158:161], v[8:11]
	s_waitcnt lgkmcnt(0)
	v_mfma_f32_16x16x32_bf16 v[46:49], v[106:109], v[154:157], v[46:49]
	v_mfma_f32_16x16x32_bf16 v[8:11], v[106:109], v[130:133], v[8:11]
	ds_read_b64_tr_b16 v[102:103], v243 offset:49152
	ds_read_b64_tr_b16 v[104:105], v243 offset:53248
	ds_read_b64_tr_b16 v[106:107], v243 offset:57344
	ds_read_b64_tr_b16 v[108:109], v243 offset:61440
	s_waitcnt lgkmcnt(2)
	v_mfma_f32_16x16x32_bf16 v[42:45], v[102:105], v[162:165], v[42:45]
	v_mfma_f32_16x16x32_bf16 v[4:7], v[102:105], v[158:161], v[4:7]
	ds_read_b64_tr_b16 v[110:111], v244 offset:49152
	ds_read_b64_tr_b16 v[112:113], v244 offset:53248
	s_waitcnt lgkmcnt(2)
	v_mfma_f32_16x16x32_bf16 v[42:45], v[106:109], v[154:157], v[42:45]
	v_mfma_f32_16x16x32_bf16 v[4:7], v[106:109], v[130:133], v[4:7]
	ds_read_b64_tr_b16 v[104:105], v244 offset:57344
	ds_read_b64_tr_b16 v[106:107], v244 offset:61440
	s_waitcnt vmcnt(0)
	v_mfma_f32_16x16x32_bf16 v[62:65], v[126:129], v[162:165], v[62:65]
	s_waitcnt lgkmcnt(0)
	s_barrier
	v_mfma_f32_16x16x32_bf16 v[24:27], v[126:129], v[158:161], v[24:27]
	v_mfma_f32_16x16x32_bf16 v[38:41], v[110:113], v[162:165], v[38:41]
	v_mfma_f32_16x16x32_bf16 v[0:3], v[110:113], v[158:161], v[0:3]
	v_mfma_f32_16x16x32_bf16 v[66:69], v[122:125], v[154:157], v[66:69]
	v_mfma_f32_16x16x32_bf16 v[28:31], v[122:125], v[130:133], v[28:31]
	v_mfma_f32_16x16x32_bf16 v[62:65], v[114:117], v[154:157], v[62:65]
	v_mfma_f32_16x16x32_bf16 v[24:27], v[114:117], v[130:133], v[24:27]
	v_mfma_f32_16x16x32_bf16 v[38:41], v[104:107], v[154:157], v[38:41]
	v_mfma_f32_16x16x32_bf16 v[0:3], v[104:107], v[130:133], v[0:3]
	s_cbranch_scc0 .LBB0_1254
	v_mov_b32_e32 v189, v215
	v_mov_b32_e32 v198, v248
	s_nop 1
	v_permlane16_swap_b32_e32 v215, v189
	v_permlane16_swap_b32_e32 v248, v198
	v_add_f32_e32 v189, v215, v189
	v_add_f32_e32 v198, v248, v198
	v_mov_b32_e32 v217, v189
	v_mov_b32_e32 v250, v198
	s_nop 1
	v_permlane32_swap_b32_e32 v189, v217
	v_permlane32_swap_b32_e32 v198, v250
	v_add_f32_e32 v103, v189, v217
	v_add_f32_e32 v102, v198, v250
	s_setprio 0
	s_branch .LBB0_1251
